# streaming (nt) hint on the final phase's f32 output stores (written once, never re-read)
# speedup vs baseline: 1.0060x; 1.0002x over previous
; DI float bf_lo(unsigned w) { return __uint_as_float(w << 16); }
; DI float bf_hi(unsigned w) { return __uint_as_float(w & 0xffff0000u); }
; #define CMB_FENCE() do { asm volatile("" ::: "memory"); __builtin_amdgcn_sched_barrier(0); } while (0)
; #define CMB_UNPK(P) ((f32x4){bf_lo((P).x), bf_hi((P).x), bf_lo((P).y), bf_hi((P).y)})
; template <bool LAST> DI void cmb_block(bf16_t* H, const bf16_t* Y, const int* inv, const float* g2, const float* gain1, const float* shift, const float* scale, bf16_t* A, float* out, int row0, int n, int lane) {
;     ...
;         f32x4 v[8];
; #pragma unroll
;         for (int j = 0; j < 8; ++j) { const f32x4 h = (f32x4){bf_lo(hp[j].x), bf_hi(hp[j].x), bf_lo(hp[j].y), bf_hi(hp[j].y)}; v[j] = h + CMB_UNPK(gvp[j]) * acc[j]; }
;         if (LAST) {
; #pragma unroll
;             for (int j = 0; j < 8; ++j) *(f32x4*)(out + (size_t)row * DM + 4 * lane + 256 * j) = v[j];
;         } else {
;             float ss = 0.f;
; #pragma unroll
;             for (int j = 0; j < 8; ++j) ss += (v[j][0] * v[j][0] + v[j][1] * v[j][1]) + (v[j][2] * v[j][2] + v[j][3] * v[j][3]);
;             ss = wave_sum(ss);
;             const float rstd = 1.0f / sqrtf(ss * (1.0f / DM) + NORM_EPS);
;             row_store_bf16(H + (size_t)row * DM, v, lane);
; #pragma unroll
;             for (int j = 0; j < 8; ++j) { const f32x4 y = (v[j] * rstd) * CMB_UNPK(Gmp[j]) + CMB_UNPK(shp[j]);
;                 *(unsigned*)((unsigned char*)A + (size_t)row * DM + 4 * lane + 256 * j) = pk4_fp8(y[0], y[1], y[2], y[3]); }
;         }
;         CMB_FENCE();
; #pragma unroll
;         for (int j = 0; j < 8; ++j) hp[j] = hn[j];
;         iv0 = iv1; iv1 = iv2;
;     }
.LBB0_2031:
	s_add_i32 s7, s7, 1
	v_lshlrev_b32_e32 v128, 16, v58
	v_and_b32_e32 v129, 0xffff0000, v58
	v_lshlrev_b32_e32 v58, 16, v59
	v_and_b32_e32 v59, 0xffff0000, v59
	v_pk_fma_f32 v[108:109], v[108:109], v[16:17], v[128:129]
	v_lshlrev_b32_e32 v128, 16, v56
	v_and_b32_e32 v129, 0xffff0000, v56
	v_lshlrev_b32_e32 v56, 16, v57
	v_and_b32_e32 v57, 0xffff0000, v57
	v_pk_fma_f32 v[110:111], v[110:111], v[18:19], v[58:59]
	v_pk_fma_f32 v[58:59], v[106:107], v[24:25], v[56:57]
	v_pk_fma_f32 v[56:57], v[104:105], v[22:23], v[128:129]
	v_lshlrev_b32_e32 v104, 16, v50
	v_and_b32_e32 v105, 0xffff0000, v50
	v_lshlrev_b32_e32 v50, 16, v51
	v_and_b32_e32 v51, 0xffff0000, v51
	v_pk_fma_f32 v[102:103], v[102:103], v[28:29], v[50:51]
	v_lshlrev_b32_e32 v50, 16, v40
	v_and_b32_e32 v51, 0xffff0000, v40
	v_lshlrev_b32_e32 v40, 16, v41
	v_and_b32_e32 v41, 0xffff0000, v41
	v_pk_fma_f32 v[98:99], v[98:99], v[34:35], v[40:41]
	v_lshlrev_b32_e32 v40, 16, v30
	v_and_b32_e32 v41, 0xffff0000, v30
	v_lshlrev_b32_e32 v30, 16, v31
	v_and_b32_e32 v31, 0xffff0000, v31
	v_pk_fma_f32 v[94:95], v[94:95], v[38:39], v[30:31]
	v_lshlrev_b32_e32 v30, 16, v20
	v_and_b32_e32 v31, 0xffff0000, v20
	v_lshlrev_b32_e32 v20, 16, v21
	v_and_b32_e32 v21, 0xffff0000, v21
	v_pk_fma_f32 v[90:91], v[90:91], v[44:45], v[20:21]
	v_lshlrev_b32_e32 v20, 16, v14
	v_and_b32_e32 v21, 0xffff0000, v14
	s_ashr_i32 s9, s8, 31
	v_pk_fma_f32 v[100:101], v[100:101], v[26:27], v[104:105]
	v_lshlrev_b32_e32 v14, 16, v15
	v_and_b32_e32 v15, 0xffff0000, v15
	v_pk_fma_f32 v[104:105], v[82:83], v[46:47], v[20:21]
	v_lshlrev_b32_e32 v20, 16, v12
	v_and_b32_e32 v21, 0xffff0000, v12
	v_lshlrev_b32_e32 v12, 16, v13
	v_and_b32_e32 v13, 0xffff0000, v13
	s_lshl_b64 s[8:9], s[8:9], 13
	v_pk_fma_f32 v[106:107], v[86:87], v[48:49], v[14:15]
	v_pk_fma_f32 v[14:15], v[80:81], v[54:55], v[12:13]
	v_pk_fma_f32 v[12:13], v[84:85], v[52:53], v[20:21]
	v_lshl_add_u64 v[20:21], v[6:7], 0, s[8:9]
	v_pk_fma_f32 v[96:97], v[96:97], v[32:33], v[50:51]
	global_store_dwordx4 v[20:21], v[108:111], off nt
	global_store_dwordx4 v[20:21], v[56:59], off offset:1024 nt
	global_store_dwordx4 v[20:21], v[100:103], off offset:2048 nt
	global_store_dwordx4 v[20:21], v[96:99], off offset:3072 nt
	v_add_co_u32_e32 v20, vcc, s3, v20
	v_pk_fma_f32 v[92:93], v[92:93], v[36:37], v[40:41]
	s_nop 0
	v_addc_co_u32_e32 v21, vcc, 0, v21, vcc
	v_pk_fma_f32 v[88:89], v[88:89], v[42:43], v[30:31]
	global_store_dwordx4 v[20:21], v[92:95], off nt
	global_store_dwordx4 v[20:21], v[88:91], off offset:1024 nt
	global_store_dwordx4 v[20:21], v[104:107], off offset:2048 nt
	global_store_dwordx4 v[20:21], v[12:15], off offset:3072 nt
	s_cmp_lg_u32 s7, 8
	s_nop 0
	v_mov_b64_e32 v[12:13], v[68:69]
	v_mov_b64_e32 v[14:15], v[70:71]
	v_mov_b64_e32 v[20:21], v[72:73]
	v_mov_b64_e32 v[30:31], v[60:61]
	v_mov_b64_e32 v[40:41], v[62:63]
	v_mov_b64_e32 v[50:51], v[64:65]
	v_mov_b64_e32 v[56:57], v[66:67]
	v_mov_b64_e32 v[58:59], v[74:75]
	v_mov_b32_e32 v127, v9
	v_mov_b32_e32 v9, v77
	s_cbranch_scc0 .LBB0_2029
